# speedup vs baseline: 1.0100x; 1.0039x over previous
.LBB3_61:
	s_or_b64 exec, exec, s[4:5]
	s_movk_i32 s5, 0x2b0
	v_mov_b32_e32 v5, 0x15000
	v_mad_u32_u24 v206, v0, s5, v5
	v_mov_b32_e32 v5, 0x3c00
	v_cmp_eq_u32_e32 vcc, 0, v55
	s_movk_i32 s4, 0xf0
	v_mul_u32_u24_e32 v3, 56, v55
	v_cndmask_b32_e32 v208, 0, v5, vcc
	v_lshlrev_b32_e32 v5, 3, v204
	v_lshl_or_b32 v5, v195, 8, v5
	v_add_u32_e32 v209, 0x26a80, v5
	v_mov_b32_e32 v5, 0x23800
	v_mov_b32_e32 v2, 0x1fc00
	v_mad_u32_u24 v4, v204, s5, v3
	s_mov_b32 s8, 0x15000
	v_mad_u32_u24 v207, v204, s4, v5
	v_lshlrev_b32_e32 v5, 3, v205
	v_lshlrev_b32_e32 v194, 4, v205
	v_mad_u32_u24 v2, v204, s4, v2
	v_add3_u32 v210, v207, v3, v5
	v_add3_u32 v212, v4, v194, s8
	s_movk_i32 s4, 0x64
	v_mov_b32_e32 v4, 0x25600
	v_mad_u32_u24 v214, v0, s4, v4
	v_add_u32_e32 v0, 48, v210
	v_cmp_gt_u32_e64 s[4:5], 32, v1
	v_add_u32_e32 v211, v2, v194
	v_add3_u32 v217, v2, v3, v5
	v_cndmask_b32_e64 v218, v209, v0, s[4:5]
	v_mul_u32_u24_e32 v0, 0x1c0, v195
	v_or_b32_e32 v0, v0, v1
	v_lshlrev_b32_e32 v0, 4, v0
	v_mov_b32_e32 v1, 0
	v_add_u32_e32 v2, 0x1000, v0
	v_mov_b32_e32 v3, v1
	v_lshl_add_u64 v[196:197], s[0:1], 0, v[0:1]
	v_lshl_add_u64 v[198:199], s[0:1], 0, v[2:3]
	v_add_u32_e32 v2, 0x1400, v0
	v_add_u32_e32 v0, 0x1800, v0
	v_add_u32_e32 v213, 0x26280, v50
	v_lshl_add_u32 v215, v54, 4, v50
	v_lshl_add_u64 v[200:201], s[0:1], 0, v[2:3]
	v_lshl_add_u64 v[202:203], s[0:1], 0, v[0:1]
	v_mov_b32_e32 v0, v1
	v_mov_b32_e32 v2, v1
	v_mov_b32_e32 v4, v1
	v_mov_b32_e32 v5, v1
	v_mov_b32_e32 v6, v1
	v_mov_b32_e32 v7, v1
	v_mov_b32_e32 v8, v1
	v_mov_b32_e32 v9, v1
	v_mov_b32_e32 v10, v1
	v_mov_b32_e32 v11, v1
	v_mov_b32_e32 v12, v1
	v_mov_b64_e32 v[80:81], v[14:15]
	v_mov_b64_e32 v[64:65], v[14:15]
	v_mov_b64_e32 v[48:49], v[14:15]
	s_mov_b32 s14, 0
	s_mov_b32 s21, 0
	v_add_u32_e32 v216, v207, v194
	s_mov_b32 s15, 0x5040100
	s_movk_i32 s18, 0x2a0
	v_mov_b64_e32 v[78:79], v[12:13]
	v_mov_b64_e32 v[76:77], v[10:11]
	v_mov_b64_e32 v[74:75], v[8:9]
	v_mov_b64_e32 v[72:73], v[6:7]
	v_mov_b64_e32 v[70:71], v[4:5]
	v_mov_b64_e32 v[68:69], v[2:3]
	v_mov_b64_e32 v[66:67], v[0:1]
	v_mov_b64_e32 v[62:63], v[12:13]
	v_mov_b64_e32 v[60:61], v[10:11]
	v_mov_b64_e32 v[58:59], v[8:9]
	v_mov_b64_e32 v[56:57], v[6:7]
	v_mov_b64_e32 v[54:55], v[4:5]
	v_mov_b64_e32 v[52:53], v[2:3]
	v_mov_b64_e32 v[50:51], v[0:1]
	v_mov_b64_e32 v[46:47], v[12:13]
	v_mov_b64_e32 v[44:45], v[10:11]
	v_mov_b64_e32 v[42:43], v[8:9]
	v_mov_b64_e32 v[40:41], v[6:7]
	v_mov_b64_e32 v[38:39], v[4:5]
	v_mov_b64_e32 v[36:37], v[2:3]
	v_mov_b64_e32 v[34:35], v[0:1]
	v_mov_b32_e32 v13, v1
	v_mov_b32_e32 v14, v1
	v_mov_b32_e32 v15, v1
	v_mov_b32_e32 v16, v1
	v_mov_b32_e32 v17, v1
	v_mov_b32_e32 v18, v1
	v_mov_b32_e32 v19, v1
	v_mov_b32_e32 v20, v1
	v_mov_b32_e32 v21, v1
	v_mov_b32_e32 v22, v1
	v_mov_b32_e32 v23, v1
	v_mov_b32_e32 v24, v1
	v_mov_b32_e32 v25, v1
	v_mov_b32_e32 v26, v1
	v_mov_b32_e32 v27, v1
	v_mov_b32_e32 v28, v1
	v_mov_b32_e32 v29, v1
	v_mov_b32_e32 v30, v1
	v_lshlrev_b32_e32 v240, 1, v192
	v_sub_u32_e32 v241, v190, v192
	v_lshlrev_b32_e32 v241, 1, v241
	v_add_u32_e32 v242, v206, v240
	v_lshl_add_u32 v243, v190, 1, v206
	s_cmp_eq_u32 s47, 2
	s_cbranch_scc1 .Lgru_restore
	s_cmp_lt_u32 s72, 0x100
	s_cbranch_scc1 .Lapf_skip_a
	ds_read_b128 v[232:235], v215
	ds_read_b128 v[236:239], v215 offset:7168
	ds_read_b128 v[240:243], v215 offset:14336
	ds_read_b128 v[244:247], v215 offset:1024
	ds_read_b128 v[200:203], v215 offset:8192
